# wt4+awr + attention: K ds_reads issued right after the barrier, before the next-unit prefetch/address block (hides that block under the K-read latency)
# baseline (speedup 1.0000x reference)
.LBB0_412:
	s_and_b32 s49, s38, 1
	s_mul_i32 s101, s49, 0x12000
	v_add3_u32 v56, s101, v182, v215
	v_add3_u32 v64, s101, v183, v215
	ds_read_b128 v[52:55], v56
	ds_read_b128 v[56:59], v56 offset:64
	ds_read_b128 v[60:63], v64
	ds_read_b128 v[66:69], v64 offset:64
	v_add3_u32 v64, s101, v184, v215
	ds_read_b128 v[70:73], v64
	ds_read_b128 v[74:77], v64 offset:64
	v_add3_u32 v64, s101, v185, v215
	ds_read_b128 v[90:93], v64
	ds_read_b128 v[94:97], v64 offset:64
	v_add3_u32 v64, s101, v186, v215
	ds_read_b128 v[98:101], v64
	ds_read_b128 v[102:105], v64 offset:64
	v_add3_u32 v64, s101, v187, v215
	ds_read_b128 v[106:109], v64
	ds_read_b128 v[110:113], v64 offset:64
	v_add3_u32 v64, s101, v188, v215
	ds_read_b128 v[114:117], v64
	ds_read_b128 v[118:121], v64 offset:64
	v_add3_u32 v64, s101, v189, v215
	ds_read_b128 v[122:125], v64
	ds_read_b128 v[126:129], v64 offset:64
	v_add3_u32 v64, s101, v190, v215
	ds_read_b128 v[130:133], v64
	ds_read_b128 v[134:137], v64 offset:64
	s_mul_hi_i32 s23, s39, 0x2aaaaaab
	s_lshr_b32 s24, s23, 31
	s_ashr_i32 s23, s23, 5
	s_add_i32 s34, s23, s24
	s_mul_i32 s23, s34, 0xffffff40
	s_add_i32 s23, s39, s23
	s_mov_b32 s31, s25
	s_and_b32 s49, s38, 1
	s_xor_b32 s100, s49, 1
	s_mul_i32 s100, s100, 0x12000
	s_ashr_i32 s24, s23, 6
	s_and_b32 s25, s39, 63
	s_ashr_i32 s36, s34, 4
	s_cmp_eq_u32 s24, 1
	s_cselect_b64 s[26:27], -1, 0
	s_and_b64 s[28:29], s[26:27], exec
	s_cselect_b32 s35, 3, 15
	s_cselect_b32 s37, 2, 4
	s_cmp_lt_u32 s23, 64
	s_cselect_b64 s[28:29], -1, 0
	s_and_b64 s[56:57], s[28:29], exec
	s_cselect_b32 s62, 0, s37
	s_waitcnt vmcnt(2)
	v_mov_b64_e32 v[88:89], v[10:11]
	s_cselect_b32 s23, 0, s35
	s_lshr_b32 s25, s25, s62
	s_waitcnt vmcnt(1)
	v_mov_b64_e32 v[50:51], v[14:15]
	v_mov_b64_e32 v[86:87], v[8:9]
	v_sub_u32_e64 v8, s25, 1 clamp
	v_mov_b64_e32 v[48:49], v[12:13]
	s_ashr_i32 s35, s34, 31
	v_lshlrev_b32_e32 v12, 7, v8
	s_and_b32 s23, s23, s70
	s_lshl_b64 s[56:57], s[34:35], 13
	v_or_b32_e32 v8, v12, v172
	s_or_b32 s56, s56, s23
	v_lshlrev_b32_e32 v64, s62, v8
	v_lshl_add_u64 v[8:9], s[56:57], 0, v[64:65]
	v_lshlrev_b64 v[8:9], 7, v[8:9]
	v_or_b32_e32 v8, v8, v191
	v_lshl_add_u64 v[10:11], s[76:77], 0, v[8:9]
	v_lshl_add_u64 v[8:9], s[78:79], 0, v[8:9]
	global_load_dwordx4 v[16:19], v[10:11], off
	global_load_dwordx4 v[20:23], v[8:9], off
	v_or_b32_e32 v8, v12, v174
	v_lshlrev_b32_e32 v64, s62, v8
	v_lshl_add_u64 v[8:9], s[56:57], 0, v[64:65]
	v_lshlrev_b64 v[8:9], 7, v[8:9]
	v_or_b32_e32 v8, v8, v191
	v_lshl_add_u64 v[10:11], s[76:77], 0, v[8:9]
	v_lshl_add_u64 v[8:9], s[78:79], 0, v[8:9]
	s_lshl_b32 s63, s25, 7
	global_load_dwordx4 v[24:27], v[10:11], off
	global_load_dwordx4 v[28:31], v[8:9], off
	v_or_b32_e32 v8, s63, v172
	v_lshlrev_b32_e32 v64, s62, v8
	v_lshl_add_u64 v[8:9], s[56:57], 0, v[64:65]
	v_lshlrev_b64 v[8:9], 7, v[8:9]
	v_or_b32_e32 v8, v8, v191
	v_lshl_add_u64 v[10:11], s[76:77], 0, v[8:9]
	v_lshl_add_u64 v[8:9], s[78:79], 0, v[8:9]
	global_load_dwordx4 v[32:35], v[10:11], off
	global_load_dwordx4 v[36:39], v[8:9], off
	v_or_b32_e32 v8, s63, v175
	v_lshlrev_b32_e32 v64, s62, v8
	v_lshl_add_u64 v[8:9], s[56:57], 0, v[64:65]
	v_lshlrev_b64 v[8:9], 7, v[8:9]
	v_or_b32_e32 v8, v8, v191
	v_lshl_add_u64 v[10:11], s[76:77], 0, v[8:9]
	v_lshl_add_u64 v[8:9], s[78:79], 0, v[8:9]
	global_load_dwordx4 v[40:43], v[10:11], off
	global_load_dwordx4 v[44:47], v[8:9], off
	s_ashr_i32 s37, s36, 31
	v_add_u32_e32 v8, s63, v181
	s_lshl_b64 s[36:37], s[36:37], 13
	v_ashrrev_i32_e32 v9, 31, v8
	s_or_b32 s36, s36, s23
	v_lshlrev_b64 v[8:9], s62, v[8:9]
	v_lshl_add_u64 v[164:165], s[36:37], 0, v[8:9]
	v_lshlrev_b64 v[162:163], 6, v[164:165]
	s_lshl_b64 s[36:37], s[34:35], 20
	s_add_u32 s36, s64, s36
	v_lshlrev_b32_e32 v8, 1, v162
	s_addc_u32 s37, s65, s37
	v_and_b32_e32 v64, 0xfff80, v8
	v_lshl_add_u64 v[8:9], s[36:37], 0, v[64:65]
	v_mov_b32_e32 v169, v65
	v_lshl_add_u64 v[12:13], v[8:9], 0, v[168:169]
	global_load_dwordx4 v[8:11], v[12:13], off
	s_nop 0
	global_load_dwordx4 v[12:15], v[12:13], off offset:64
	s_waitcnt lgkmcnt(14)
	v_mfma_f32_16x16x32_bf16 v[52:55], v[52:55], v[86:89], v[4:7]
	s_cmp_lg_u32 s31, 0
	v_mfma_f32_16x16x32_bf16 v[82:85], v[56:59], v[48:51], v[52:55]
	v_mfma_f32_16x16x32_bf16 v[52:55], v[60:63], v[86:89], 0
	v_mfma_f32_16x16x32_bf16 v[78:81], v[66:69], v[48:51], v[52:55]
	s_waitcnt lgkmcnt(13)
	v_mfma_f32_16x16x32_bf16 v[52:55], v[70:73], v[86:89], 0
	s_waitcnt lgkmcnt(12)
	v_mfma_f32_16x16x32_bf16 v[74:77], v[74:77], v[48:51], v[52:55]
	s_waitcnt lgkmcnt(11)
	v_mfma_f32_16x16x32_bf16 v[52:55], v[90:93], v[86:89], 0
	s_waitcnt lgkmcnt(10)
	v_mfma_f32_16x16x32_bf16 v[70:73], v[94:97], v[48:51], v[52:55]
	s_waitcnt lgkmcnt(9)
	v_mfma_f32_16x16x32_bf16 v[52:55], v[98:101], v[86:89], 0
	s_waitcnt lgkmcnt(8)
	v_mfma_f32_16x16x32_bf16 v[66:69], v[102:105], v[48:51], v[52:55]
	s_waitcnt lgkmcnt(7)
	v_mfma_f32_16x16x32_bf16 v[52:55], v[106:109], v[86:89], 0
	s_waitcnt lgkmcnt(6)
	v_mfma_f32_16x16x32_bf16 v[60:63], v[110:113], v[48:51], v[52:55]
	s_waitcnt lgkmcnt(5)
	v_mfma_f32_16x16x32_bf16 v[52:55], v[114:117], v[86:89], 0
	s_waitcnt lgkmcnt(4)
	v_mfma_f32_16x16x32_bf16 v[56:59], v[118:121], v[48:51], v[52:55]
	s_waitcnt lgkmcnt(3)
	v_mfma_f32_16x16x32_bf16 v[52:55], v[122:125], v[86:89], 0
	s_waitcnt lgkmcnt(1)
	v_mfma_f32_16x16x32_bf16 v[86:89], v[130:133], v[86:89], v[0:3]
	v_mfma_f32_16x16x32_bf16 v[52:55], v[126:129], v[48:51], v[52:55]
	s_waitcnt lgkmcnt(0)
	v_mfma_f32_16x16x32_bf16 v[48:51], v[134:137], v[48:51], v[86:89]
	s_cbranch_scc1 .LBB0_414
	s_nop 3
	v_pk_add_f32 v[86:87], v[84:85], s[84:85] op_sel_hi:[1,0]
	v_pk_add_f32 v[88:89], v[82:83], s[84:85] op_sel_hi:[1,0]
	v_cndmask_b32_e64 v85, v85, v87, s[20:21]
	v_cndmask_b32_e64 v84, v84, v86, s[20:21]
	v_cndmask_b32_e64 v83, v83, v89, s[20:21]
	v_cndmask_b32_e64 v82, v82, v88, s[20:21]
	v_pk_add_f32 v[86:87], v[80:81], s[84:85] op_sel_hi:[1,0]
	v_pk_add_f32 v[88:89], v[78:79], s[84:85] op_sel_hi:[1,0]
	v_cndmask_b32_e64 v81, v81, v87, s[18:19]
	v_cndmask_b32_e64 v80, v80, v86, s[18:19]
	v_cndmask_b32_e64 v79, v79, v89, s[18:19]
	v_cndmask_b32_e64 v78, v78, v88, s[18:19]
	v_pk_add_f32 v[86:87], v[76:77], s[84:85] op_sel_hi:[1,0]
	v_pk_add_f32 v[88:89], v[74:75], s[84:85] op_sel_hi:[1,0]
	v_cndmask_b32_e64 v77, v77, v87, s[16:17]
	v_cndmask_b32_e64 v76, v76, v86, s[16:17]
	v_cndmask_b32_e64 v75, v75, v89, s[16:17]
	v_cndmask_b32_e64 v74, v74, v88, s[16:17]
	v_pk_add_f32 v[86:87], v[72:73], s[84:85] op_sel_hi:[1,0]
	v_pk_add_f32 v[88:89], v[70:71], s[84:85] op_sel_hi:[1,0]
	v_cndmask_b32_e64 v73, v73, v87, s[14:15]
	v_cndmask_b32_e64 v72, v72, v86, s[14:15]
	v_cndmask_b32_e64 v71, v71, v89, s[14:15]
	v_cndmask_b32_e64 v70, v70, v88, s[14:15]
	v_pk_add_f32 v[86:87], v[68:69], s[84:85] op_sel_hi:[1,0]
	v_pk_add_f32 v[88:89], v[66:67], s[84:85] op_sel_hi:[1,0]
	v_cndmask_b32_e64 v69, v69, v87, s[12:13]
	v_cndmask_b32_e64 v68, v68, v86, s[12:13]
	v_cndmask_b32_e64 v67, v67, v89, s[12:13]
	v_cndmask_b32_e64 v66, v66, v88, s[12:13]
	v_pk_add_f32 v[86:87], v[62:63], s[84:85] op_sel_hi:[1,0]
	v_pk_add_f32 v[88:89], v[60:61], s[84:85] op_sel_hi:[1,0]
	v_cndmask_b32_e64 v63, v63, v87, s[10:11]
	v_cndmask_b32_e64 v62, v62, v86, s[10:11]
	v_cndmask_b32_e64 v61, v61, v89, s[10:11]
	v_cndmask_b32_e64 v60, v60, v88, s[10:11]
	v_pk_add_f32 v[86:87], v[58:59], s[84:85] op_sel_hi:[1,0]
	v_pk_add_f32 v[88:89], v[56:57], s[84:85] op_sel_hi:[1,0]
	v_cndmask_b32_e64 v59, v59, v87, s[8:9]
	v_cndmask_b32_e64 v58, v58, v86, s[8:9]
	v_cndmask_b32_e64 v57, v57, v89, s[8:9]
	v_cndmask_b32_e64 v56, v56, v88, s[8:9]
	v_pk_add_f32 v[86:87], v[54:55], s[84:85] op_sel_hi:[1,0]
	v_pk_add_f32 v[88:89], v[52:53], s[84:85] op_sel_hi:[1,0]
	v_cndmask_b32_e64 v55, v55, v87, s[6:7]
	v_cndmask_b32_e64 v54, v54, v86, s[6:7]
	v_cndmask_b32_e64 v53, v53, v89, s[6:7]
	v_cndmask_b32_e64 v52, v52, v88, s[6:7]
.LBB0_414:
	v_add3_u32 v64, s101, v173, v171
	ds_read_b64_tr_b16 v[90:91], v64 offset:36864
	s_nop 1
	ds_read_b64_tr_b16 v[86:87], v64 offset:36896
	ds_read_b64_tr_b16 v[100:101], v64 offset:36928
	ds_read_b64_tr_b16 v[108:109], v64 offset:36960
	ds_read_b64_tr_b16 v[92:93], v64 offset:39168
	ds_read_b64_tr_b16 v[88:89], v64 offset:39200
	ds_read_b64_tr_b16 v[102:103], v64 offset:39232
	ds_read_b64_tr_b16 v[110:111], v64 offset:39264
	ds_read_b64_tr_b16 v[104:105], v64 offset:41472
	ds_read_b64_tr_b16 v[112:113], v64 offset:41504
	ds_read_b64_tr_b16 v[118:119], v64 offset:41536
	ds_read_b64_tr_b16 v[126:127], v64 offset:41568
	ds_read_b64_tr_b16 v[106:107], v64 offset:43776
	ds_read_b64_tr_b16 v[114:115], v64 offset:43808
	ds_read_b64_tr_b16 v[120:121], v64 offset:43840
	ds_read_b64_tr_b16 v[128:129], v64 offset:43872
	ds_read_b64_tr_b16 v[122:123], v64 offset:46080
	ds_read_b64_tr_b16 v[130:131], v64 offset:46112
	ds_read_b64_tr_b16 v[138:139], v64 offset:46144
	ds_read_b64_tr_b16 v[146:147], v64 offset:46176
	ds_read_b64_tr_b16 v[124:125], v64 offset:48384
	ds_read_b64_tr_b16 v[132:133], v64 offset:48416
	ds_read_b64_tr_b16 v[140:141], v64 offset:48448
	ds_read_b64_tr_b16 v[148:149], v64 offset:48480
	ds_read_b64_tr_b16 v[142:143], v64 offset:50688
	ds_read_b64_tr_b16 v[152:153], v64 offset:50720
	ds_read_b64_tr_b16 v[156:157], v64 offset:50752
	ds_read_b64_tr_b16 v[134:135], v64 offset:50784
	ds_read_b64_tr_b16 v[144:145], v64 offset:52992
	ds_read_b64_tr_b16 v[154:155], v64 offset:53024
	ds_read_b64_tr_b16 v[158:159], v64 offset:53056
	ds_read_b64_tr_b16 v[136:137], v64 offset:53088
	ds_read_b64_tr_b16 v[150:151], v64 offset:55296
	ds_read_b64_tr_b16 v[116:117], v64 offset:55328
	ds_read_b64_tr_b16 v[98:99], v64 offset:55360
	ds_read_b64_tr_b16 v[94:95], v64 offset:55392
	v_max3_f32 v64, v82, s84, v83
	v_max3_f32 v64, v64, v84, v85
	v_max3_f32 v64, v64, v78, v79
	v_max3_f32 v64, v64, v80, v81
	v_max3_f32 v64, v64, v74, v75
	v_max3_f32 v64, v64, v76, v77
	v_max3_f32 v64, v64, v70, v71
	v_max3_f32 v64, v64, v72, v73
	v_max3_f32 v64, v64, v66, v67
	v_max3_f32 v64, v64, v68, v69
	v_max3_f32 v64, v64, v60, v61
	v_max3_f32 v64, v64, v62, v63
	v_max3_f32 v64, v64, v56, v57
	v_max3_f32 v64, v64, v58, v59
	v_max3_f32 v64, v64, v52, v53
	v_max3_f32 v64, v64, v54, v55
	v_max3_f32 v64, v64, v48, v49
	v_max3_f32 v64, v64, v50, v51
	v_mov_b32_e32 v96, v64
	s_nop 1
	v_permlane16_swap_b32_e32 v64, v96
	v_max_f32_e32 v96, v96, v96
	v_max_f32_e32 v64, v64, v64
	v_max_f32_e32 v64, v64, v96
	v_mov_b32_e32 v96, v64
	s_nop 1
	v_permlane32_swap_b32_e32 v64, v96
	v_max_f32_e32 v96, v96, v96
	v_max_f32_e32 v64, v64, v64
	v_max_f32_e32 v170, v64, v96
	v_pk_add_f32 v[82:83], v[82:83], v[170:171] op_sel_hi:[1,0] neg_lo:[0,1] neg_hi:[0,1]
	v_pk_add_f32 v[84:85], v[84:85], v[170:171] op_sel_hi:[1,0] neg_lo:[0,1] neg_hi:[0,1]
	v_exp_f32_e32 v82, v82
	v_exp_f32_e32 v83, v83
	v_exp_f32_e32 v84, v84
	v_exp_f32_e32 v85, v85
	v_pk_add_f32 v[78:79], v[78:79], v[170:171] op_sel_hi:[1,0] neg_lo:[0,1] neg_hi:[0,1]
	v_pk_add_f32 v[80:81], v[80:81], v[170:171] op_sel_hi:[1,0] neg_lo:[0,1] neg_hi:[0,1]
	v_exp_f32_e32 v78, v78
	v_exp_f32_e32 v79, v79
	v_exp_f32_e32 v80, v80
	v_exp_f32_e32 v81, v81
	v_pk_add_f32 v[74:75], v[74:75], v[170:171] op_sel_hi:[1,0] neg_lo:[0,1] neg_hi:[0,1]
	v_pk_add_f32 v[96:97], v[82:83], 0 op_sel_hi:[1,0]
	v_pk_add_f32 v[76:77], v[76:77], v[170:171] op_sel_hi:[1,0] neg_lo:[0,1] neg_hi:[0,1]
	v_exp_f32_e32 v192, v74
	v_exp_f32_e32 v193, v75
	v_pk_add_f32 v[96:97], v[84:85], v[96:97]
	v_exp_f32_e32 v194, v76
	v_exp_f32_e32 v195, v77
	v_pk_add_f32 v[70:71], v[70:71], v[170:171] op_sel_hi:[1,0] neg_lo:[0,1] neg_hi:[0,1]
	v_pk_add_f32 v[74:75], v[78:79], v[96:97]
	v_pk_add_f32 v[72:73], v[72:73], v[170:171] op_sel_hi:[1,0] neg_lo:[0,1] neg_hi:[0,1]
	v_exp_f32_e32 v96, v70
	v_exp_f32_e32 v97, v71
	v_pk_add_f32 v[74:75], v[80:81], v[74:75]
	v_exp_f32_e32 v196, v72
	v_exp_f32_e32 v197, v73
	v_pk_add_f32 v[66:67], v[66:67], v[170:171] op_sel_hi:[1,0] neg_lo:[0,1] neg_hi:[0,1]
	v_pk_add_f32 v[74:75], v[192:193], v[74:75]
	v_pk_add_f32 v[68:69], v[68:69], v[170:171] op_sel_hi:[1,0] neg_lo:[0,1] neg_hi:[0,1]
	v_exp_f32_e32 v198, v66
	v_exp_f32_e32 v199, v67
	v_pk_add_f32 v[74:75], v[194:195], v[74:75]
	v_exp_f32_e32 v200, v68
	v_exp_f32_e32 v201, v69
	v_pk_add_f32 v[66:67], v[96:97], v[74:75]
	v_cvt_pk_bf16_f32 v68, v78, v79
	v_pk_add_f32 v[66:67], v[196:197], v[66:67]
	v_cvt_pk_bf16_f32 v69, v80, v81
	v_pk_add_f32 v[66:67], v[198:199], v[66:67]
	v_pk_add_f32 v[74:75], v[60:61], v[170:171] op_sel_hi:[1,0] neg_lo:[0,1] neg_hi:[0,1]
	v_pk_add_f32 v[202:203], v[200:201], v[66:67]
	v_cvt_pk_bf16_f32 v66, v82, v83
	v_cvt_pk_bf16_f32 v67, v84, v85
	v_pk_add_f32 v[76:77], v[62:63], v[170:171] op_sel_hi:[1,0] neg_lo:[0,1] neg_hi:[0,1]
	v_exp_f32_e32 v78, v74
	s_waitcnt lgkmcnt(14)
	v_mfma_f32_16x16x32_bf16 v[70:73], v[90:93], v[66:69], 0
	v_exp_f32_e32 v79, v75
	v_exp_f32_e32 v80, v76
	v_exp_f32_e32 v81, v77
	v_mfma_f32_16x16x32_bf16 v[60:63], v[86:89], v[66:69], 0
	v_add_f32_e64 v84, v56, -v170
	v_add_f32_e64 v85, v57, -v170
	v_pk_add_f32 v[86:87], v[58:59], v[170:171] op_sel_hi:[1,0] neg_lo:[0,1] neg_hi:[0,1]
	v_exp_f32_e32 v84, v84
	v_mfma_f32_16x16x32_bf16 v[74:77], v[100:103], v[66:69], 0
	v_exp_f32_e32 v85, v85
	v_exp_f32_e32 v86, v86
	v_exp_f32_e32 v87, v87
	v_mfma_f32_16x16x32_bf16 v[56:59], v[108:111], v[66:69], 0
	v_cvt_pk_bf16_f32 v66, v192, v193
	v_cvt_pk_bf16_f32 v67, v194, v195
	v_cvt_pk_bf16_f32 v68, v96, v97
	v_cvt_pk_bf16_f32 v69, v196, v197
	v_pk_add_f32 v[88:89], v[52:53], v[170:171] op_sel_hi:[1,0] neg_lo:[0,1] neg_hi:[0,1]
	v_pk_add_f32 v[82:83], v[78:79], v[202:203]
	v_mfma_f32_16x16x32_bf16 v[70:73], v[104:107], v[66:69], v[70:73]
	v_add_f32_e64 v90, v54, -v170
	v_add_f32_e64 v91, v55, -v170
	v_pk_add_f32 v[82:83], v[80:81], v[82:83]
	v_pk_add_f32 v[48:49], v[48:49], v[170:171] op_sel_hi:[1,0] neg_lo:[0,1] neg_hi:[0,1]
	v_mfma_f32_16x16x32_bf16 v[60:63], v[112:115], v[66:69], v[60:63]
	v_add_f32_e64 v82, v84, v82
	v_add_f32_e64 v83, v85, v83
	s_waitcnt lgkmcnt(1)
	v_mov_b32_e32 v100, v98
	v_pk_add_f32 v[82:83], v[86:87], v[82:83]
	v_mfma_f32_16x16x32_bf16 v[74:77], v[118:121], v[66:69], v[74:77]
	v_mov_b32_e32 v118, v116
	v_mov_b32_e32 v119, v117
	v_mov_b32_e32 v101, v99
	v_mfma_f32_16x16x32_bf16 v[52:55], v[126:129], v[66:69], v[56:59]
	s_waitcnt lgkmcnt(0)
	v_mov_b32_e32 v96, v94
	v_mov_b32_e32 v97, v95
	v_mov_b32_e32 v64, v65
	v_cvt_pk_bf16_f32 v58, v78, v79
	v_exp_f32_e32 v78, v88
	v_exp_f32_e32 v79, v89
	v_cvt_pk_bf16_f32 v56, v198, v199
	v_cvt_pk_bf16_f32 v57, v200, v201
	v_cvt_pk_bf16_f32 v59, v80, v81
	v_exp_f32_e32 v80, v90
	v_exp_f32_e32 v81, v91
	v_mfma_f32_16x16x32_bf16 v[66:69], v[122:125], v[56:59], v[70:73]
	v_add_f32_e64 v82, v78, v82
	v_add_f32_e64 v83, v79, v83
	s_cmp_eq_u32 s30, 1
	s_mov_b32 s23, 0xe800000
	v_mfma_f32_16x16x32_bf16 v[60:63], v[130:133], v[56:59], v[60:63]
	s_cselect_b32 s23, s23, 0x2e800000
	s_cmp_lg_u32 s30, 0
	s_cselect_b32 s23, s23, 0x12800000
	v_mfma_f32_16x16x32_bf16 v[70:73], v[138:141], v[56:59], v[74:77]
	s_add_u32 s36, s42, s23
	s_addc_u32 s37, s43, 0
	s_lshl_b32 s66, s22, 6
	v_pk_add_f32 v[74:75], v[50:51], v[170:171] op_sel_hi:[1,0] neg_lo:[0,1] neg_hi:[0,1]
	v_exp_f32_e32 v76, v48
	v_exp_f32_e32 v77, v49
	v_exp_f32_e32 v74, v74
	v_exp_f32_e32 v75, v75
	v_mfma_f32_16x16x32_bf16 v[48:51], v[146:149], v[56:59], v[52:55]
	s_nop 2
	v_cvt_pk_bf16_f32 v52, v84, v85
	v_cvt_pk_bf16_f32 v53, v86, v87
	v_cvt_pk_bf16_f32 v54, v78, v79
	v_cvt_pk_bf16_f32 v55, v80, v81
	v_pk_add_f32 v[78:79], v[80:81], v[82:83]
	s_nop 0
	v_mfma_f32_16x16x32_bf16 v[56:59], v[142:145], v[52:55], v[66:69]
	v_mfma_f32_16x16x32_bf16 v[66:69], v[152:155], v[52:55], v[60:63]
	v_mov_b32_e32 v152, v150
	v_mov_b32_e32 v153, v151
	s_nop 0
	v_pk_add_f32 v[60:61], v[76:77], v[78:79]
	v_mfma_f32_16x16x32_bf16 v[70:73], v[156:159], v[52:55], v[70:73]
	v_add_f32_e64 v60, v74, v60
	v_add_f32_e64 v61, v75, v61
	v_cvt_pk_bf16_f32 v62, v76, v77
	v_pk_add_f32 v[60:61], v[60:61], v[60:61] op_sel:[0,1] op_sel_hi:[1,0]
	v_mfma_f32_16x16x32_bf16 v[48:51], v[134:137], v[52:55], v[48:51]
	v_mov_b32_e32 v61, v60
	s_nop 1
	v_permlane16_swap_b32_e32 v60, v61
	v_cvt_pk_bf16_f32 v63, v74, v75
	v_add_f32_e32 v74, v60, v61
	s_nop 0
	v_mfma_f32_16x16x32_bf16 v[52:55], v[150:153], v[62:65], v[56:59]
	v_mfma_f32_16x16x32_bf16 v[56:59], v[116:119], v[62:65], v[66:69]
	v_mfma_f32_16x16x32_bf16 v[66:69], v[98:101], v[62:65], v[70:73]
	s_nop 2
	v_mov_b32_e32 v70, v74
	s_nop 1
	v_permlane32_swap_b32_e32 v74, v70
	v_mfma_f32_16x16x32_bf16 v[60:63], v[94:97], v[62:65], v[48:51]
	s_nop 2
	v_add_f32_e32 v48, v74, v70
	v_rcp_f32_e32 v49, v48
	s_nop 0
	v_mul_f32_e32 v49, 0x42800000, v49
	v_add3_u32 v206, s100, v177, v176
	s_waitcnt vmcnt(9)
	ds_write_b128 v206, v[16:19]
	v_mul_f32_e32 v50, v49, v52
	v_mul_f32_e32 v51, v49, v53
	v_med3_f32 v53, v50, s55, v228
	v_med3_f32 v51, v51, s55, v228
	v_mov_b32_e32 v50, v65
	v_cvt_pk_fp8_f32 v50, v53, v51
	s_waitcnt vmcnt(8)
	ds_write_b128 v206, v[20:23] offset:36864
	v_mul_f32_e32 v52, v49, v54
	v_mul_f32_e32 v51, v49, v55
	v_med3_f32 v52, v52, s55, v228
	v_med3_f32 v51, v51, s55, v228
	v_cvt_pk_fp8_f32 v50, v52, v51 op_sel:[0,0,1]
	v_add3_u32 v206, s100, v178, v176
	s_waitcnt vmcnt(7)
	ds_write_b128 v206, v[24:27]
	v_mul_f32_e32 v51, v49, v56
	v_mul_f32_e32 v52, v49, v57
	v_med3_f32 v54, v51, s55, v228
	v_med3_f32 v52, v52, s55, v228
	v_mov_b32_e32 v51, v65
	v_cvt_pk_fp8_f32 v51, v54, v52
	s_waitcnt vmcnt(6)
	ds_write_b128 v206, v[28:31] offset:36864
	v_mul_f32_e32 v53, v49, v58
	v_mul_f32_e32 v52, v49, v59
	v_med3_f32 v53, v53, s55, v228
	v_med3_f32 v52, v52, s55, v228
	v_cvt_pk_fp8_f32 v51, v53, v52 op_sel:[0,0,1]
	v_add3_u32 v206, s100, v179, v176
	s_waitcnt vmcnt(5)
	ds_write_b128 v206, v[32:35]
	v_mul_f32_e32 v52, v49, v66
	v_mul_f32_e32 v53, v49, v67
	v_med3_f32 v55, v52, s55, v228
	v_med3_f32 v53, v53, s55, v228
	v_mov_b32_e32 v52, v65
	v_cvt_pk_fp8_f32 v52, v55, v53
	s_waitcnt vmcnt(4)
	ds_write_b128 v206, v[36:39] offset:36864
	v_mul_f32_e32 v54, v49, v68
	v_mul_f32_e32 v53, v49, v69
	v_med3_f32 v54, v54, s55, v228
	v_med3_f32 v53, v53, s55, v228
	v_cvt_pk_fp8_f32 v52, v54, v53 op_sel:[0,0,1]
	v_add3_u32 v206, s100, v180, v176
	s_waitcnt vmcnt(3)
	ds_write_b128 v206, v[40:43]
	v_mul_f32_e32 v53, v49, v60
	v_mul_f32_e32 v54, v49, v61
	v_med3_f32 v56, v53, s55, v228
	v_med3_f32 v54, v54, s55, v228
	v_mov_b32_e32 v53, v65
	v_cvt_pk_fp8_f32 v53, v56, v54
	s_waitcnt vmcnt(2)
	ds_write_b128 v206, v[44:47] offset:36864
	v_mul_f32_e32 v55, v49, v62
	v_mul_f32_e32 v49, v49, v63
	v_med3_f32 v54, v55, s55, v228
	v_med3_f32 v49, v49, s55, v228
	v_cvt_pk_fp8_f32 v53, v54, v49 op_sel:[0,0,1]
	v_lshlrev_b64 v[54:55], 10, v[166:167]
	v_lshl_add_u64 v[54:55], s[36:37], 0, v[54:55]
	v_lshl_add_u64 v[54:55], v[54:55], 0, s[66:67]
	v_lshl_add_u64 v[54:55], v[54:55], 0, v[160:161]
	global_store_dwordx4 v[54:55], v[50:53], off sc1
	s_and_saveexec_b64 s[36:37], vcc
	s_cbranch_execz .LBB0_416
	v_log_f32_e32 v48, v48
	s_ashr_i32 s31, s30, 31
	s_lshl_b64 s[30:31], s[30:31], 22
	v_readlane_b32 s23, v254, 30
	s_add_u32 s30, s23, s30
	v_readlane_b32 s23, v254, 31
	v_add_f32_e32 v48, v170, v48
	s_addc_u32 s31, s23, s31
	v_mul_f32_e32 v50, 0x3f317218, v48
	v_lshlrev_b64 v[48:49], 6, v[166:167]
	v_lshl_add_u64 v[48:49], s[30:31], 0, v[48:49]
	s_mov_b32 s23, s67
	v_lshl_add_u64 v[48:49], s[22:23], 2, v[48:49]
	global_store_dword v[48:49], v50, off
